# gdnprep: second half-workgroup numbers its waves in reverse so that wave-asymmetric stages of the two halves use different SIMDs
# speedup vs baseline: 1.0104x; 1.0011x over previous
; DI int tidx() { int t = threadIdx.x & 255; asm volatile("" : "+v"(t)); return t; }
; DI void gdn_prep_unit(const Params& p, int U, char* lds) {
;   const int tid = tidx(), lane = tid & 63, wid = tid >> 6, fr = lane & 15, fq = lane >> 4;
;   const int b = U >> 9, h = (U >> 7) & 3, c = U & 127;
;   const size_t t0 = (size_t)b * S_ + c * 64;
;   const int s0 = c * 64;
;   const bf16_t* proj = (const bf16_t*)(p.ws + WS_P);
;   const float* small = (const float*)(p.ws + WS_SMALL);
;   bf16_t* q_s = (bf16_t*)lds; bf16_t* k_s = q_s + 64 * QP; bf16_t* v_s = k_s + 64 * QP;
;   float* Lm = (float*)(lds + 3 * 17408);
;   bf16_t* T1 = (bf16_t*)Lm; bf16_t* T2 = T1 + 64 * 72;
;   float* gcs = (float*)(lds + 3 * 17408 + 18432);
;   bf16_t* QF = (bf16_t*)((char*)p.out) + (size_t)U * 8192;
;   bf16_t* KF = (bf16_t*)((char*)p.out + 32 * MiB) + (size_t)U * 8192;
;   bf16_t* AF = (bf16_t*)((char*)p.out + 64 * MiB) + (size_t)U * 4096;
;   bf16_t* UF = (bf16_t*)(p.ws + WS_UF) + (size_t)U * 8192;
;   bf16_t* WF = (bf16_t*)(p.ws + WS_WF) + (size_t)U * 8192;
; DI void phase_gdnprep(const Params& p, int bid, int nb, char* lds) {
;   for (int U = bid; U < 2048; U += nb) gdn_prep_unit(p, U, lds);
; }
.LBB0_1086:
	s_or_b64 exec, exec, s[4:5]
	v_lshrrev_b32_e32 v249, 8, v207
	v_mul_u32_u24_e32 v249, 0xc0, v249
	v_xor_b32_e32 v206, v206, v249
	s_movk_i32 s2, 0x800
	v_cmp_gt_i32_e64 s[4:5], s2, v176
	s_and_saveexec_b64 s[16:17], s[4:5]
	s_cbranch_execz .LBB0_1155
	s_add_u32 s26, s66, 0x2000000
	s_addc_u32 s27, s67, 0
	s_add_u32 s28, s66, 0x4000000
	s_addc_u32 s29, s67, 0
	s_add_u32 s30, s84, 0x1a00000
	s_addc_u32 s31, s85, 0
	s_add_u32 s34, s84, 0x1e000000
	s_addc_u32 s35, s85, 0
	v_add_u32_e32 v0, 0, v190
	v_mbcnt_hi_u32_b32 v123, -1, v177
	s_add_u32 s38, s84, 0x1c000000
	v_add_u32_e32 v26, 0xcc00, v0
	v_add_u32_e32 v28, 0xee00, v0
	v_add_u32_e32 v111, 0x2080, v0
	v_add_u32_e32 v117, 0x80, v0
	v_and_b32_e32 v165, 64, v123
	s_mov_b32 s0, 0x358637bd
	v_bfrev_b32_e32 v0, 0.5
	v_add_u32_e32 v29, 0x11400, v146
	v_add_u32_e32 v105, 0x11800, v146
	s_addc_u32 s39, s85, 0
	s_mov_b64 s[40:41], 0
	v_mov_b32_e32 v30, 0
	s_movk_i32 s3, 0x2c00
	v_xor_b32_e32 v164, 4, v123
	v_add_u32_e32 v166, 64, v165
	s_mov_b32 s42, 0x3db504f3
	s_movk_i32 s18, 0x110
	s_mov_b32 s19, 0x800000
	s_movk_i32 s22, 0x88
	s_mov_b32 s23, 0x5040100
	s_movk_i32 s43, 0x440
	s_movk_i32 s68, 0x48
	s_movk_i32 s69, 0x90
	s_movk_i32 s72, 0x7ff
	v_add_u32_e32 v167, -1, v123
	v_add_u32_e32 v168, -2, v123
	v_add_u32_e32 v169, -4, v123
	v_add_u32_e32 v170, -8, v123
	v_add_u32_e32 v171, -16, v123
	v_subrev_u32_e32 v172, 32, v123
	v_lshl_or_b32 v173, v123, 2, v0
	v_mov_b64_e32 v[32:33], s[0:1]
	v_mov_b32_e32 v174, 0x1100
	v_mov_b32_e32 v34, v176
	s_branch .LBB0_1089

; DI int tidx() { int t = threadIdx.x & 255; asm volatile("" : "+v"(t)); return t; }
; DI void phase_foxcum(const Params& p, int bid, int nb, char* lds) {
;   float* tot = (float*)lds;
;   const float* small = (const float*)(p.ws + WS_SMALL);
;   float* fneg = (float*)(p.ws + WS_FNEG);
;   const int tid = tidx();
;   for (int bh = bid; bh < 32; bh += nb) {
;     const int b = bh >> 3, h = bh & 7;
;     float v[32]; float run = 0.f;
; #pragma unroll
;     for (int i = 0; i < 32; ++i) { run += small[((size_t)b * S_ + tid * 32 + i) * 16 + h]; v[i] = run; }
;     tot[tid] = run; __syncthreads();
;     float off = 0.f; for (int j = 0; j < tid; ++j) off += tot[j];
; #pragma unroll
;     for (int i = 0; i < 32; ++i) fneg[(size_t)bh * S_ + tid * 32 + i] = -(v[i] + off) * LOG2E;
.LBB0_1155:
	s_or_b64 exec, exec, s[16:17]
	v_xor_b32_e32 v206, v206, v249
	v_readfirstlane_b32 s26, v176
	v_readfirstlane_b32 s27, v206
	s_lshr_b32 s27, s27, 6
	v_mbcnt_lo_u32_b32 v0, -1, 0
	v_mbcnt_hi_u32_b32 v0, -1, v0
	v_lshrrev_b32_e32 v1, 5, v0
	v_and_b32_e32 v2, 31, v0
	v_lshl_add_u32 v3, s27, 1, v1
	s_lshl_b32 s28, s26, 6
	v_lshl_add_u32 v4, v2, 1, s28
	v_lshlrev_b32_e32 v4, 6, v4
	v_lshl_add_u32 v4, v3, 2, v4
	s_add_u32 s30, s84, 0x1700000
	s_addc_u32 s31, s85, 0
	global_load_dword v5, v4, s[30:31]
	global_load_dword v6, v4, s[30:31] offset:64
	s_and_b32 s34, s26, 127
	s_lshr_b32 s35, s26, 7
	s_lshl_b32 s38, s35, 13
	s_add_u32 s38, s38, 0x8000
	s_add_u32 s38, s84, s38
	s_addc_u32 s39, s85, 0
	v_lshlrev_b32_e32 v10, 6, v2
	v_lshl_add_u32 v10, v3, 3, v10
	v_add_u32_e32 v11, 0x1000, v10
	s_sub_u32 s40, s34, 32
	s_sub_u32 s41, s34, 64
	s_sub_u32 s42, s34, 0x60
	s_mov_b32 s43, 0
